# v4
# speedup vs baseline: 1.0047x; 1.0047x over previous
.LBB7_4:
	s_abs_i32 s3, s10
	v_cvt_f32_u32_e32 v1, s3
	s_sub_i32 s15, 0, s3
	s_add_i32 s2, s6, s2
	s_abs_i32 s7, s2
	v_rcp_iflag_f32_e32 v1, v1
	s_xor_b32 s6, s2, s10
	s_ashr_i32 s6, s6, 31
	s_load_dwordx2 s[0:1], s[0:1], 0x18
	v_mul_f32_e32 v1, 0x4f7ffffe, v1
	v_cvt_u32_f32_e32 v1, v1
	v_bfe_u32 v52, v0, 6, 1
	v_bfe_u32 v42, v0, 4, 2
	v_lshrrev_b32_e32 v43, 7, v0
	v_readfirstlane_b32 s18, v1
	s_mul_i32 s15, s15, s18
	s_mul_hi_u32 s15, s18, s15
	s_add_i32 s18, s18, s15
	s_mul_hi_u32 s15, s7, s18
	s_mul_i32 s18, s15, s3
	s_sub_i32 s7, s7, s18
	s_add_i32 s19, s15, 1
	s_sub_i32 s18, s7, s3
	s_cmp_ge_u32 s7, s3
	s_cselect_b32 s15, s19, s15
	s_cselect_b32 s7, s18, s7
	s_add_i32 s18, s15, 1
	s_cmp_ge_u32 s7, s3
	s_cselect_b32 s3, s18, s15
	s_abs_i32 s7, s11
	v_cvt_f32_u32_e32 v1, s7
	s_xor_b32 s3, s3, s6
	s_sub_i32 s3, s3, s6
	s_mul_i32 s6, s3, s10
	v_rcp_iflag_f32_e32 v1, v1
	s_sub_i32 s19, s2, s6
	s_sub_i32 s6, 0, s7
	s_xor_b32 s2, s19, s11
	v_mul_f32_e32 v1, 0x4f7ffffe, v1
	v_cvt_u32_f32_e32 v1, v1
	s_ashr_i32 s18, s2, 31
	s_abs_i32 s2, s19
	v_lshlrev_b32_e32 v6, 4, v42
	v_readfirstlane_b32 s10, v1
	s_mul_i32 s6, s6, s10
	s_mul_hi_u32 s6, s10, s6
	s_add_i32 s10, s10, s6
	s_mul_hi_u32 s6, s2, s10
	s_mul_i32 s10, s6, s7
	s_sub_i32 s2, s2, s10
	s_add_i32 s10, s6, 1
	s_sub_i32 s15, s2, s7
	s_cmp_ge_u32 s2, s7
	s_cselect_b32 s6, s10, s6
	s_cselect_b32 s2, s15, s2
	s_add_i32 s10, s6, 1
	s_cmp_ge_u32 s2, s7
	s_cselect_b32 s2, s10, s6
	s_xor_b32 s20, s2, s18
	s_ashr_i32 s2, s14, 31
	v_lshrrev_b32_e32 v1, 3, v0
	s_lshr_b32 s2, s2, 26
	v_mul_lo_u32 v2, s14, v1
	v_xor_b32_e32 v1, v1, v0
	s_add_i32 s2, s14, s2
	v_lshlrev_b32_e32 v1, 3, v1
	s_sub_i32 s22, s20, s18
	s_ashr_i32 s15, s2, 6
	v_and_b32_e32 v1, 56, v1
	s_lshl_b32 s24, s22, 6
	s_mul_i32 s21, s15, s3
	v_add_lshl_u32 v44, v2, v1, 1
	v_lshlrev_b32_e32 v1, 4, v0
	s_lshl_b32 s3, s21, 6
	v_add_u32_e32 v45, 0, v1
	s_mul_i32 s23, s24, s14
	s_mul_i32 s2, s12, s14
	s_add_i32 s26, s23, s3
	v_readfirstlane_b32 s27, v45
	v_readfirstlane_b32 s32, v45
	s_lshl_b32 s6, s2, 1
	s_and_b32 s5, s5, 0xffff
	s_mov_b32 s7, 0x20000
	s_lshl_b32 s26, s26, 1
	s_mov_b32 m0, s27
	s_mul_i32 s22, s22, s11
	buffer_load_dwordx4 v44, s[4:7], s26 offen lds
	s_lshl_b32 s26, s14, 5
	s_mul_i32 s2, s13, s14
	s_sub_i32 s12, s19, s22
	v_add_u32_e32 v2, 0x1000, v45
	s_add_i32 s27, s23, s26
	s_lshl_b32 s10, s2, 1
	s_mul_i32 s2, s12, 0x60
	s_add_i32 s28, s27, s3
	v_readfirstlane_b32 s29, v2
	s_mul_i32 s25, s2, s14
	s_lshl_b32 s28, s28, 1
	s_mov_b32 m0, s29
	v_add_u32_e32 v2, 0x2000, v45
	buffer_load_dwordx4 v44, s[4:7], s28 offen lds
	s_add_i32 s28, s25, s3
	v_readfirstlane_b32 s29, v2
	s_and_b32 s9, s9, 0xffff
	s_mov_b32 s11, s7
	s_lshl_b32 s28, s28, 1
	s_mov_b32 m0, s29
	v_add_u32_e32 v2, 0x3000, v45
	buffer_load_dwordx4 v44, s[8:11], s28 offen lds
	s_add_i32 s28, s25, s26
	s_add_i32 s29, s28, s3
	v_readfirstlane_b32 s30, v2
	s_lshl_b32 s29, s29, 1
	s_mov_b32 m0, s30
	v_add_u32_e32 v2, 0x4000, v45
	s_add_i32 s26, s28, s26
	buffer_load_dwordx4 v44, s[8:11], s29 offen lds
	s_add_i32 s29, s26, s3
	v_readfirstlane_b32 s30, v2
	s_lshl_b32 s29, s29, 1
	s_mov_b32 m0, s30
	v_add_u32_e32 v2, 0x5000, v45
	buffer_load_dwordx4 v44, s[8:11], s29 offen lds
	s_add_i32 s29, s3, 64
	s_add_i32 s30, s23, s29
	v_readfirstlane_b32 s31, v2
	s_lshl_b32 s30, s30, 1
	s_mov_b32 m0, s31
	v_add_u32_e32 v2, 0x6000, v45
	buffer_load_dwordx4 v44, s[4:7], s30 offen lds
	s_add_i32 s30, s27, s29
	v_readfirstlane_b32 s31, v2
	s_lshl_b32 s30, s30, 1
	s_mov_b32 m0, s31
	v_add_u32_e32 v2, 0x7000, v45
	buffer_load_dwordx4 v44, s[4:7], s30 offen lds
	s_add_i32 s30, s25, s29
	v_readfirstlane_b32 s31, v2
	s_lshl_b32 s30, s30, 1
	s_mov_b32 m0, s31
	v_add_u32_e32 v2, 0x8000, v45
	buffer_load_dwordx4 v44, s[8:11], s30 offen lds
	s_add_i32 s30, s28, s29
	v_readfirstlane_b32 s31, v2
	s_lshl_b32 s30, s30, 1
	s_mov_b32 m0, s31
	v_add_u32_e32 v2, 0x9000, v45
	buffer_load_dwordx4 v44, s[8:11], s30 offen lds
	s_add_i32 s29, s26, s29
	v_readfirstlane_b32 s30, v2
	s_lshl_b32 s29, s29, 1
	s_mov_b32 m0, s30
	v_add_u32_e32 v2, 0xa000, v45
	buffer_load_dwordx4 v44, s[8:11], s29 offen lds
	s_add_i32 s29, s3, 0x80
	s_add_i32 s30, s23, s29
	v_readfirstlane_b32 s31, v2
	s_lshl_b32 s30, s30, 1
	s_mov_b32 m0, s31
	v_add_u32_e32 v2, 0xb000, v45
	buffer_load_dwordx4 v44, s[4:7], s30 offen lds
	s_add_i32 s30, s27, s29
	v_readfirstlane_b32 s31, v2
	s_lshl_b32 s30, s30, 1
	s_mov_b32 m0, s31
	v_add_u32_e32 v2, 0xc000, v45
	buffer_load_dwordx4 v44, s[4:7], s30 offen lds
	s_add_i32 s30, s25, s29
	v_readfirstlane_b32 s31, v2
	s_lshl_b32 s30, s30, 1
	s_mov_b32 m0, s31
	v_add_u32_e32 v2, 0xd000, v45
	buffer_load_dwordx4 v44, s[8:11], s30 offen lds
	s_add_i32 s30, s28, s29
	v_readfirstlane_b32 s31, v2
	s_lshl_b32 s30, s30, 1
	s_mov_b32 m0, s31
	v_add_u32_e32 v2, 0xe000, v45
	buffer_load_dwordx4 v44, s[8:11], s30 offen lds
	s_add_i32 s29, s26, s29
	v_readfirstlane_b32 s30, v2
	s_lshl_b32 s29, s29, 1
	s_mov_b32 m0, s30
	v_add_u32_e32 v2, 0xf000, v45
	buffer_load_dwordx4 v44, s[8:11], s29 offen lds
	s_add_i32 s29, s3, 0xc0
	s_add_i32 s30, s23, s29
	v_readfirstlane_b32 s31, v2
	s_lshl_b32 s30, s30, 1
	s_mov_b32 m0, s31
	v_add_u32_e32 v2, 0x10000, v45
	buffer_load_dwordx4 v44, s[4:7], s30 offen lds
	s_add_i32 s30, s27, s29
	v_readfirstlane_b32 s31, v2
	s_lshl_b32 s30, s30, 1
	s_mov_b32 m0, s31
	v_and_b32_e32 v53, 15, v0
	buffer_load_dwordx4 v44, s[4:7], s30 offen lds
	s_add_i32 s30, 0, 0x11000
	v_add_u32_e32 v2, s30, v1
	s_add_i32 s30, s25, s29
	v_readfirstlane_b32 s31, v2
	s_lshl_b32 s30, s30, 1
	s_mov_b32 m0, s31
	v_add_u32_e32 v3, 0x1000, v2
	buffer_load_dwordx4 v44, s[8:11], s30 offen lds
	s_add_i32 s30, s28, s29
	v_readfirstlane_b32 s31, v3
	s_lshl_b32 s30, s30, 1
	s_mov_b32 m0, s31
	v_add_u32_e32 v2, 0x2000, v2
	buffer_load_dwordx4 v44, s[8:11], s30 offen lds
	s_add_i32 s29, s26, s29
	v_readfirstlane_b32 s30, v2
	s_lshl_b32 s29, s29, 1
	s_mov_b32 m0, s30
	v_accvgpr_write_b32 a0, 0
	buffer_load_dwordx4 v44, s[8:11], s29 offen lds
	s_add_i32 s29, 0, 0x14000
	v_add_u32_e32 v2, s29, v1
	s_add_i32 s29, s3, 0x100
	s_add_i32 s30, s23, s29
	v_readfirstlane_b32 s31, v2
	s_lshl_b32 s30, s30, 1
	s_mov_b32 m0, s31
	v_add_u32_e32 v2, 0x1000, v2
	buffer_load_dwordx4 v44, s[4:7], s30 offen lds
	s_add_i32 s30, s27, s29
	v_readfirstlane_b32 s31, v2
	s_lshl_b32 s30, s30, 1
	s_mov_b32 m0, s31
	v_accvgpr_write_b32 a1, 0
	buffer_load_dwordx4 v44, s[4:7], s30 offen lds
	s_add_i32 s30, 0, 0x16000
	v_add_u32_e32 v2, s30, v1
	s_add_i32 s30, s25, s29
	v_readfirstlane_b32 s31, v2
	s_lshl_b32 s30, s30, 1
	s_mov_b32 m0, s31
	v_add_u32_e32 v3, 0x1000, v2
	buffer_load_dwordx4 v44, s[8:11], s30 offen lds
	s_add_i32 s30, s28, s29
	v_readfirstlane_b32 s31, v3
	s_lshl_b32 s30, s30, 1
	s_mov_b32 m0, s31
	v_add_u32_e32 v2, 0x2000, v2
	buffer_load_dwordx4 v44, s[8:11], s30 offen lds
	s_add_i32 s29, s26, s29
	v_readfirstlane_b32 s30, v2
	s_lshl_b32 s29, s29, 1
	s_mov_b32 m0, s30
	v_accvgpr_write_b32 a2, 0
	buffer_load_dwordx4 v44, s[8:11], s29 offen lds
	s_add_i32 s29, 0, 0x19000
	v_add_u32_e32 v2, s29, v1
	s_add_i32 s29, s3, 0x140
	s_add_i32 s30, s23, s29
	v_readfirstlane_b32 s31, v2
	s_lshl_b32 s30, s30, 1
	s_mov_b32 m0, s31
	v_add_u32_e32 v2, 0x1000, v2
	buffer_load_dwordx4 v44, s[4:7], s30 offen lds
	s_add_i32 s30, s27, s29
	v_readfirstlane_b32 s31, v2
	s_lshl_b32 s30, s30, 1
	s_mov_b32 m0, s31
	s_addk_i32 s3, 0x180
	buffer_load_dwordx4 v44, s[4:7], s30 offen lds
	s_add_i32 s30, 0, 0x1b000
	v_add_u32_e32 v2, s30, v1
	s_add_i32 s30, s25, s29
	v_readfirstlane_b32 s31, v2
	s_lshl_b32 s30, s30, 1
	s_mov_b32 m0, s31
	v_add_u32_e32 v3, 0x1000, v2
	buffer_load_dwordx4 v44, s[8:11], s30 offen lds
	s_add_i32 s30, s28, s29
	v_readfirstlane_b32 s31, v3
	s_lshl_b32 s30, s30, 1
	s_mov_b32 m0, s31
	v_add_u32_e32 v2, 0x2000, v2
	buffer_load_dwordx4 v44, s[8:11], s30 offen lds
	s_add_i32 s29, s26, s29
	v_readfirstlane_b32 s30, v2
	s_lshl_b32 s29, s29, 1
	s_mov_b32 m0, s30
	s_add_i32 s27, s27, s3
	buffer_load_dwordx4 v44, s[8:11], s29 offen lds
	s_add_i32 s29, 0, 0x1e000
	v_add_u32_e32 v2, s29, v1
	s_add_i32 s29, s23, s3
	v_readfirstlane_b32 s30, v2
	s_lshl_b32 s29, s29, 1
	s_mov_b32 m0, s30
	v_add_u32_e32 v2, 0x1000, v2
	buffer_load_dwordx4 v44, s[4:7], s29 offen lds
	v_readfirstlane_b32 s29, v2
	s_lshl_b32 s27, s27, 1
	s_mov_b32 m0, s29
	s_add_i32 s25, s25, s3
	buffer_load_dwordx4 v44, s[4:7], s27 offen lds
	s_add_i32 s27, 0, 0x20000
	v_add_u32_e32 v1, s27, v1
	v_add_u32_e32 v2, 0x1000, v1
	v_readfirstlane_b32 s27, v1
	s_lshl_b32 s25, s25, 1
	s_mov_b32 m0, s27
	s_add_i32 s28, s28, s3
	v_readfirstlane_b32 s27, v2
	buffer_load_dwordx4 v44, s[8:11], s25 offen lds
	s_lshl_b32 s25, s28, 1
	s_mov_b32 m0, s27
	v_add_u32_e32 v1, 0x2000, v1
	buffer_load_dwordx4 v44, s[8:11], s25 offen lds
	s_add_i32 s26, s26, s3
	v_readfirstlane_b32 s25, v1
	s_lshl_b32 s3, s26, 1
	s_mov_b32 m0, s25
	v_mul_u32_u24_e32 v1, 48, v52
	buffer_load_dwordx4 v44, s[8:11], s3 offen lds
	s_ashr_i32 s3, s2, 31
	s_lshl_b64 s[26:27], s[2:3], 2
	s_add_u32 s16, s16, s26
	s_addc_u32 s17, s17, s27
	v_lshlrev_b32_e32 v2, 2, v1
	v_mov_b32_e32 v3, 0
	v_lshl_add_u64 v[4:5], s[16:17], 0, v[2:3]
	v_mov_b32_e32 v7, v3
	s_waitcnt lgkmcnt(0)
	s_add_u32 s16, s0, s26
	v_lshl_add_u64 v[46:47], v[4:5], 0, v[6:7]
	v_lshlrev_b32_e32 v4, 5, v43
	s_addc_u32 s17, s1, s27
	v_or3_b32 v4, s24, v4, v53
	v_lshl_add_u64 v[2:3], s[16:17], 0, v[2:3]
	v_lshl_add_u64 v[2:3], v[2:3], 0, v[6:7]
	v_mad_i64_i32 v[40:41], s[16:17], v4, s13, 0
	v_or_b32_e32 v4, 16, v4
	v_lshl_add_u64 v[48:49], v[40:41], 2, v[2:3]
	v_mad_i64_i32 v[38:39], s[16:17], v4, s13, 0
	global_load_dwordx4 v[34:37], v[48:49], off
	global_load_dwordx4 v[30:33], v[48:49], off offset:64
	v_lshl_add_u64 v[50:51], v[38:39], 2, v[2:3]
	global_load_dwordx4 v[26:29], v[48:49], off offset:128
	global_load_dwordx4 v[18:21], v[50:51], off
	global_load_dwordx4 v[22:25], v[46:47], off
	global_load_dwordx4 v[10:13], v[46:47], off offset:64
	global_load_dwordx4 v[2:5], v[46:47], off offset:128
	global_load_dwordx4 v[14:17], v[50:51], off offset:64
	global_load_dwordx4 v[6:9], v[50:51], off offset:128
	v_lshrrev_b32_e32 v46, 4, v0
	v_and_b32_e32 v0, 7, v0
	v_bitop3_b32 v46, v46, v0, 3 bitop3:0x6c
	v_bitop3_b32 v0, v42, v0, 4 bitop3:0x36
	v_lshlrev_b32_e32 v47, 6, v53
	s_add_i32 s3, s15, -6
	s_mov_b32 s13, 0
	v_lshl_or_b32 v46, v46, 3, v47
	v_accvgpr_write_b32 a3, 0
	v_accvgpr_write_b32 a4, 0
	v_accvgpr_write_b32 a5, 0
	v_accvgpr_write_b32 a6, 0
	v_accvgpr_write_b32 a7, 0
	v_accvgpr_write_b32 a8, 0
	v_accvgpr_write_b32 a9, 0
	v_accvgpr_write_b32 a10, 0
	v_accvgpr_write_b32 a11, 0
	v_accvgpr_write_b32 a12, 0
	v_accvgpr_write_b32 a13, 0
	v_accvgpr_write_b32 a14, 0
	v_accvgpr_write_b32 a15, 0
	v_accvgpr_write_b32 a16, 0
	v_accvgpr_write_b32 a17, 0
	v_accvgpr_write_b32 a18, 0
	v_accvgpr_write_b32 a19, 0
	v_accvgpr_write_b32 a20, 0
	v_accvgpr_write_b32 a21, 0
	v_accvgpr_write_b32 a22, 0
	v_accvgpr_write_b32 a23, 0
	v_lshl_or_b32 v47, v0, 3, v47
	s_cmpk_lt_i32 s14, 0x1c0
	v_lshlrev_b32_e32 v0, 12, v43
	v_mul_u32_u24_e32 v43, 0x1800, v52
	s_cbranch_scc1 .LBB7_9
	s_mulk_i32 s19, 0x60
	s_mulk_i32 s22, 0x60
	s_sub_i32 s11, s19, s22
	s_add_i32 s17, s11, 64
	s_add_i32 s11, s11, 32
	s_mul_i32 s11, s14, s11
	s_lshl_b32 s19, s21, 7
	s_lshl_b32 s21, s11, 1
	s_mul_i32 s11, s14, s12
	s_mul_i32 s12, s11, 0xc0
	s_lshl_b32 s11, s20, 6
	s_lshl_b32 s18, s18, 6
	s_sub_i32 s11, s11, s18
	s_or_b32 s11, s11, 32
	s_mul_i32 s17, s14, s17
	s_mul_i32 s11, s14, s11
	s_lshl_b32 s17, s17, 1
	s_lshl_b32 s14, s11, 1
	s_lshl_b32 s18, s23, 1
	s_max_i32 s16, s3, 1
	s_addk_i32 s17, 0x380
	s_addk_i32 s21, 0x380
	s_addk_i32 s12, 0x380
	s_addk_i32 s14, 0x380
	s_addk_i32 s18, 0x380
	v_accvgpr_write_b32 a23, 0
	v_accvgpr_write_b32 a22, 0
	v_accvgpr_write_b32 a21, 0
	v_accvgpr_write_b32 a20, 0
	v_accvgpr_write_b32 a19, 0
	v_accvgpr_write_b32 a18, 0
	v_accvgpr_write_b32 a17, 0
	v_accvgpr_write_b32 a16, 0
	v_accvgpr_write_b32 a15, 0
	v_accvgpr_write_b32 a14, 0
	v_accvgpr_write_b32 a13, 0
	v_accvgpr_write_b32 a12, 0
	v_accvgpr_write_b32 a11, 0
	v_accvgpr_write_b32 a10, 0
	v_accvgpr_write_b32 a9, 0
	v_accvgpr_write_b32 a8, 0
	v_accvgpr_write_b32 a7, 0
	v_accvgpr_write_b32 a6, 0
	v_accvgpr_write_b32 a5, 0
	v_accvgpr_write_b32 a4, 0
	v_accvgpr_write_b32 a3, 0
	v_accvgpr_write_b32 a2, 0
	v_accvgpr_write_b32 a1, 0
	v_accvgpr_write_b32 a0, 0
	s_branch .LBB7_7

.LBB7_7:
	s_waitcnt vmcnt(30)
	s_add_i32 s11, s13, 7
	s_cmp_ge_i32 s11, s15
	s_barrier
	s_cbranch_scc1 .LBB7_6
	s_and_b32 s11, s11, 7
	s_mulk_i32 s11, 0x5000
	s_add_i32 s33, s32, s11
	s_add_i32 s34, s18, s19
	s_add_i32 s35, s14, s19
	s_add_i32 s36, s12, s19
	s_add_i32 s37, s21, s19
	s_add_i32 s38, s17, s19
	s_and_b32 s39, s13, 7
	s_mulk_i32 s39, 0x5000
	v_add_u32_e32 v72, s39, v43
	v_lshlrev_b32_e32 v52, 1, v46
	v_add_u32_e32 v68, s39, v0
	v_add_u32_e32 v64, v72, v52
	v_add_u32_e32 v60, v68, v52
	ds_read_b128 v[48:51], v64 offset:8192
	ds_read_b128 v[52:55], v60
	ds_read_b128 v[56:59], v64 offset:10240
	ds_read_b128 v[60:63], v60 offset:2048
	ds_read_b128 v[64:67], v64 offset:12288
	v_lshlrev_b32_e32 v73, 1, v47
	s_mov_b32 m0, s33
	s_add_i32 s13, s13, 1
	s_addk_i32 s19, 0x80
	buffer_load_dwordx4 v44, s[4:7], s34 offen lds
	s_add_i32 s33, s33, 0x1000
	s_waitcnt lgkmcnt(2)
	v_mfma_f32_16x16x32_f16 a[4:7], v[56:59], v[52:55], a[4:7]
	v_add_u32_e32 v74, v68, v73
	ds_read_b128 v[68:71], v74
	s_mov_b32 m0, s33
	s_waitcnt lgkmcnt(2)
	v_mfma_f32_16x16x32_f16 a[16:19], v[56:59], v[60:63], a[16:19]
	v_add_u32_e32 v56, v72, v73
	buffer_load_dwordx4 v44, s[4:7], s35 offen lds
	s_add_i32 s33, s33, 0x1000
	v_mfma_f32_16x16x32_f16 a[0:3], v[48:51], v[52:55], a[0:3]
	s_mov_b32 m0, s33
	s_mov_b32 s11, s7
	s_waitcnt lgkmcnt(1)
	v_mfma_f32_16x16x32_f16 a[8:11], v[64:67], v[52:55], a[8:11]
	ds_read_b128 v[52:55], v56 offset:10240
	buffer_load_dwordx4 v44, s[8:11], s36 offen lds
	s_add_i32 s33, s33, 0x1000
	v_mfma_f32_16x16x32_f16 a[12:15], v[48:51], v[60:63], a[12:15]
	ds_read_b128 v[48:51], v56 offset:8192
	ds_read_b128 v[56:59], v56 offset:12288
	s_mov_b32 m0, s33
	v_mfma_f32_16x16x32_f16 a[20:23], v[64:67], v[60:63], a[20:23]
	ds_read_b128 v[60:63], v74 offset:2048
	buffer_load_dwordx4 v44, s[8:11], s37 offen lds
	s_add_i32 s33, s33, 0x1000
	s_waitcnt lgkmcnt(2)
	v_mfma_f32_16x16x32_f16 a[0:3], v[48:51], v[68:71], a[0:3]
	s_mov_b32 m0, s33
	v_mfma_f32_16x16x32_f16 a[4:7], v[52:55], v[68:71], a[4:7]
	buffer_load_dwordx4 v44, s[8:11], s38 offen lds
	s_waitcnt lgkmcnt(1)
	v_mfma_f32_16x16x32_f16 a[8:11], v[56:59], v[68:71], a[8:11]
	s_waitcnt lgkmcnt(0)
	v_mfma_f32_16x16x32_f16 a[12:15], v[48:51], v[60:63], a[12:15]
	v_mfma_f32_16x16x32_f16 a[16:19], v[52:55], v[60:63], a[16:19]
	s_cmp_lg_u32 s16, s13
	v_mfma_f32_16x16x32_f16 a[20:23], v[56:59], v[60:63], a[20:23]
	s_cbranch_scc1 .LBB7_7
	s_branch .LBB7_9

	.amdhsa_kernel _Z7gemm_tnILi64ELi96ELi2ELi2ELi8ELi2ELi1EEvPKDF16_S1_PKfPfPDF16_iiiiiS3_S3_S4_
		.amdhsa_group_segment_fixed_size 0
		.amdhsa_private_segment_fixed_size 0
		.amdhsa_kernarg_size 88
		.amdhsa_user_sgpr_count 2
		.amdhsa_user_sgpr_dispatch_ptr 0
		.amdhsa_user_sgpr_queue_ptr 0
		.amdhsa_user_sgpr_kernarg_segment_ptr 1
		.amdhsa_user_sgpr_dispatch_id 0
		.amdhsa_user_sgpr_kernarg_preload_length 0
		.amdhsa_user_sgpr_kernarg_preload_offset 0
		.amdhsa_user_sgpr_private_segment_size 0
		.amdhsa_uses_dynamic_stack 0
		.amdhsa_enable_private_segment 0
		.amdhsa_system_sgpr_workgroup_id_x 1
		.amdhsa_system_sgpr_workgroup_id_y 0
		.amdhsa_system_sgpr_workgroup_id_z 0
		.amdhsa_system_sgpr_workgroup_info 0
		.amdhsa_system_vgpr_workitem_id 0
		.amdhsa_next_free_vgpr 100
		.amdhsa_next_free_sgpr 40
		.amdhsa_accum_offset 76
		.amdhsa_reserve_vcc 0
		.amdhsa_float_round_mode_32 0
		.amdhsa_float_round_mode_16_64 0
		.amdhsa_float_denorm_mode_32 3
		.amdhsa_float_denorm_mode_16_64 3
		.amdhsa_dx10_clamp 1
		.amdhsa_ieee_mode 1
		.amdhsa_fp16_overflow 0
		.amdhsa_tg_split 0
		.amdhsa_exception_fp_ieee_invalid_op 0
		.amdhsa_exception_fp_denorm_src 0
		.amdhsa_exception_fp_ieee_div_zero 0
		.amdhsa_exception_fp_ieee_overflow 0
		.amdhsa_exception_fp_ieee_underflow 0
		.amdhsa_exception_fp_ieee_inexact 0
		.amdhsa_exception_int_div_zero 0
	.end_amdhsa_kernel

amdhsa.kernels:
  - .agpr_count:     0
    .args:
      - .actual_access:  read_only
        .address_space:  global
        .offset:         0
        .size:           8
        .value_kind:     global_buffer
      - .actual_access:  write_only
        .address_space:  global
        .offset:         8
        .size:           8
        .value_kind:     global_buffer
      - .offset:         16
        .size:           4
        .value_kind:     by_value
      - .offset:         20
        .size:           4
        .value_kind:     by_value
      - .offset:         24
        .size:           4
        .value_kind:     by_value
    .group_segment_fixed_size: 17408
    .kernarg_segment_align: 8
    .kernarg_segment_size: 28
    .language:       OpenCL C
    .language_version:
      - 2
      - 0
    .max_flat_workgroup_size: 256
    .name:           _Z13conv_w_kernelPKfPDF16_iii
    .private_segment_fixed_size: 0
    .sgpr_count:     23
    .sgpr_spill_count: 0
    .symbol:         _Z13conv_w_kernelPKfPDF16_iii.kd
    .uniform_work_group_size: 1
    .uses_dynamic_stack: false
    .vgpr_count:     52
    .vgpr_spill_count: 0
    .wavefront_size: 64
  - .agpr_count:     0
    .args:
      - .offset:         0
        .size:           264
        .value_kind:     by_value
    .group_segment_fixed_size: 17408
    .kernarg_segment_align: 8
    .kernarg_segment_size: 264
    .language:       OpenCL C
    .language_version:
      - 2
      - 0
    .max_flat_workgroup_size: 256
    .name:           _Z15conv_all_kernel7ConvJob
    .private_segment_fixed_size: 0
    .sgpr_count:     78
    .sgpr_spill_count: 0
    .symbol:         _Z15conv_all_kernel7ConvJob.kd
    .uniform_work_group_size: 1
    .uses_dynamic_stack: false
    .vgpr_count:     62
    .vgpr_spill_count: 0
    .wavefront_size: 64
  - .agpr_count:     0
    .args:
      - .actual_access:  read_only
        .address_space:  global
        .offset:         0
        .size:           8
        .value_kind:     global_buffer
      - .actual_access:  read_only
        .address_space:  global
        .offset:         8
        .size:           8
        .value_kind:     global_buffer
      - .actual_access:  read_only
        .address_space:  global
        .offset:         16
        .size:           8
        .value_kind:     global_buffer
      - .actual_access:  read_only
        .address_space:  global
        .offset:         24
        .size:           8
        .value_kind:     global_buffer
      - .actual_access:  read_only
        .address_space:  global
        .offset:         32
        .size:           8
        .value_kind:     global_buffer
      - .actual_access:  write_only
        .address_space:  global
        .offset:         40
        .size:           8
        .value_kind:     global_buffer
      - .actual_access:  write_only
        .address_space:  global
        .offset:         48
        .size:           8
        .value_kind:     global_buffer
      - .offset:         56
        .size:           264
        .value_kind:     by_value
    .group_segment_fixed_size: 17408
    .kernarg_segment_align: 8
    .kernarg_segment_size: 320
    .language:       OpenCL C
    .language_version:
      - 2
      - 0
    .max_flat_workgroup_size: 256
    .name:           _Z15embed_ln_kernelPKiPKfS2_S2_S2_PfPDF16_7ConvJob
    .private_segment_fixed_size: 0
    .sgpr_count:     74
    .sgpr_spill_count: 0
    .symbol:         _Z15embed_ln_kernelPKiPKfS2_S2_S2_PfPDF16_7ConvJob.kd
    .uniform_work_group_size: 1
    .uses_dynamic_stack: false
    .vgpr_count:     62
    .vgpr_spill_count: 0
    .wavefront_size: 64
  - .agpr_count:     0
    .args:
      - .actual_access:  read_only
        .address_space:  global
        .offset:         0
        .size:           8
        .value_kind:     global_buffer
      - .actual_access:  read_only
        .address_space:  global
        .offset:         8
        .size:           8
        .value_kind:     global_buffer
      - .actual_access:  read_only
        .address_space:  global
        .offset:         16
        .size:           8
        .value_kind:     global_buffer
      - .actual_access:  write_only
        .address_space:  global
        .offset:         24
        .size:           8
        .value_kind:     global_buffer
      - .offset:         32
        .size:           264
        .value_kind:     by_value
    .group_segment_fixed_size: 17408
    .kernarg_segment_align: 8
    .kernarg_segment_size: 296
    .language:       OpenCL C
    .language_version:
      - 2
      - 0
    .max_flat_workgroup_size: 256
    .name:           _Z9ln_kernelPKfS0_S0_PDF16_7ConvJob
    .private_segment_fixed_size: 0
    .sgpr_count:     74
    .sgpr_spill_count: 0
    .symbol:         _Z9ln_kernelPKfS0_S0_PDF16_7ConvJob.kd
    .uniform_work_group_size: 1
    .uses_dynamic_stack: false
    .vgpr_count:     62
    .vgpr_spill_count: 0
    .wavefront_size: 64
  - .agpr_count:     0
    .args:
      - .actual_access:  read_only
        .address_space:  global
        .offset:         0
        .size:           8
        .value_kind:     global_buffer
      - .actual_access:  write_only
        .address_space:  global
        .offset:         8
        .size:           8
        .value_kind:     global_buffer
      - .offset:         16
        .size:           264
        .value_kind:     by_value
    .group_segment_fixed_size: 35072
    .kernarg_segment_align: 8
    .kernarg_segment_size: 280
    .language:       OpenCL C
    .language_version:
      - 2
      - 0
    .max_flat_workgroup_size: 512
    .name:           _Z18attn_rowsum_kernelPKDF16_PDF16_7ConvJob
    .private_segment_fixed_size: 0
    .sgpr_count:     74
    .sgpr_spill_count: 0
    .symbol:         _Z18attn_rowsum_kernelPKDF16_PDF16_7ConvJob.kd
    .uniform_work_group_size: 1
    .uses_dynamic_stack: false
    .vgpr_count:     72
    .vgpr_spill_count: 0
    .wavefront_size: 64
  - .agpr_count:     0
    .args:
      - .actual_access:  read_only
        .address_space:  global
        .offset:         0
        .size:           8
        .value_kind:     global_buffer
      - .actual_access:  read_only
        .address_space:  global
        .offset:         8
        .size:           8
        .value_kind:     global_buffer
      - .actual_access:  read_only
        .address_space:  global
        .offset:         16
        .size:           8
        .value_kind:     global_buffer
      - .address_space:  global
        .offset:         24
        .size:           8
        .value_kind:     global_buffer
      - .actual_access:  write_only
        .address_space:  global
        .offset:         32
        .size:           8
        .value_kind:     global_buffer
      - .offset:         40
        .size:           4
        .value_kind:     by_value
      - .offset:         44
        .size:           4
        .value_kind:     by_value
      - .offset:         48
        .size:           4
        .value_kind:     by_value
      - .offset:         52
        .size:           4
        .value_kind:     by_value
      - .offset:         56
        .size:           4
        .value_kind:     by_value
      - .actual_access:  read_only
        .address_space:  global
        .offset:         64
        .size:           8
        .value_kind:     global_buffer
      - .actual_access:  read_only
        .address_space:  global
        .offset:         72
        .size:           8
        .value_kind:     global_buffer
      - .address_space:  global
        .offset:         80
        .size:           8
        .value_kind:     global_buffer
    .group_segment_fixed_size: 0
    .kernarg_segment_align: 8
    .kernarg_segment_size: 88
    .language:       OpenCL C
    .language_version:
      - 2
      - 0
    .max_flat_workgroup_size: 768
    .name:           _Z7gemm_tnILi128ELi144ELi4ELi3ELi4ELi0ELi1EEvPKDF16_S1_PKfPfPDF16_iiiiiS3_S3_S4_
    .private_segment_fixed_size: 0
    .sgpr_count:     37
    .sgpr_spill_count: 0
    .symbol:         _Z7gemm_tnILi128ELi144ELi4ELi3ELi4ELi0ELi1EEvPKDF16_S1_PKfPfPDF16_iiiiiS3_S3_S4_.kd
    .uniform_work_group_size: 1
    .uses_dynamic_stack: false
    .vgpr_count:     68
    .vgpr_spill_count: 0
    .wavefront_size: 64
  - .agpr_count:     0
    .args:
      - .actual_access:  read_only
        .address_space:  global
        .offset:         0
        .size:           8
        .value_kind:     global_buffer
      - .actual_access:  read_only
        .address_space:  global
        .offset:         8
        .size:           8
        .value_kind:     global_buffer
      - .actual_access:  read_only
        .address_space:  global
        .offset:         16
        .size:           8
        .value_kind:     global_buffer
      - .address_space:  global
        .offset:         24
        .size:           8
        .value_kind:     global_buffer
      - .actual_access:  write_only
        .address_space:  global
        .offset:         32
        .size:           8
        .value_kind:     global_buffer
      - .offset:         40
        .size:           4
        .value_kind:     by_value
      - .offset:         44
        .size:           4
        .value_kind:     by_value
      - .offset:         48
        .size:           4
        .value_kind:     by_value
      - .offset:         52
        .size:           4
        .value_kind:     by_value
      - .offset:         56
        .size:           4
        .value_kind:     by_value
      - .actual_access:  read_only
        .address_space:  global
        .offset:         64
        .size:           8
        .value_kind:     global_buffer
      - .actual_access:  read_only
        .address_space:  global
        .offset:         72
        .size:           8
        .value_kind:     global_buffer
      - .address_space:  global
        .offset:         80
        .size:           8
        .value_kind:     global_buffer
    .group_segment_fixed_size: 7424
    .kernarg_segment_align: 8
    .kernarg_segment_size: 88
    .language:       OpenCL C
    .language_version:
      - 2
      - 0
    .max_flat_workgroup_size: 768
    .name:           _Z7gemm_tnILi128ELi144ELi4ELi3ELi4ELi7ELi1EEvPKDF16_S1_PKfPfPDF16_iiiiiS3_S3_S4_
    .private_segment_fixed_size: 0
    .sgpr_count:     46
    .sgpr_spill_count: 0
    .symbol:         _Z7gemm_tnILi128ELi144ELi4ELi3ELi4ELi7ELi1EEvPKDF16_S1_PKfPfPDF16_iiiiiS3_S3_S4_.kd
    .uniform_work_group_size: 1
    .uses_dynamic_stack: false
    .vgpr_count:     87
    .vgpr_spill_count: 0
    .wavefront_size: 64
  - .agpr_count:     24
    .args:
      - .actual_access:  read_only
        .address_space:  global
        .offset:         0
        .size:           8
        .value_kind:     global_buffer
      - .actual_access:  read_only
        .address_space:  global
        .offset:         8
        .size:           8
        .value_kind:     global_buffer
      - .actual_access:  read_only
        .address_space:  global
        .offset:         16
        .size:           8
        .value_kind:     global_buffer
      - .address_space:  global
        .offset:         24
        .size:           8
        .value_kind:     global_buffer
      - .actual_access:  read_only
        .address_space:  global
        .offset:         32
        .size:           8
        .value_kind:     global_buffer
      - .offset:         40
        .size:           4
        .value_kind:     by_value
      - .offset:         44
        .size:           4
        .value_kind:     by_value
      - .offset:         48
        .size:           4
        .value_kind:     by_value
      - .offset:         52
        .size:           4
        .value_kind:     by_value
      - .offset:         56
        .size:           4
        .value_kind:     by_value
      - .actual_access:  read_only
        .address_space:  global
        .offset:         64
        .size:           8
        .value_kind:     global_buffer
      - .actual_access:  read_only
        .address_space:  global
        .offset:         72
        .size:           8
        .value_kind:     global_buffer
      - .address_space:  global
        .offset:         80
        .size:           8
        .value_kind:     global_buffer
    .group_segment_fixed_size: 0
    .kernarg_segment_align: 8
    .kernarg_segment_size: 88
    .language:       OpenCL C
    .language_version:
      - 2
      - 0
    .max_flat_workgroup_size: 256
    .name:           _Z7gemm_tnILi64ELi96ELi2ELi2ELi8ELi2ELi1EEvPKDF16_S1_PKfPfPDF16_iiiiiS3_S3_S4_
    .private_segment_fixed_size: 0
    .sgpr_count:     46
    .sgpr_spill_count: 0
    .symbol:         _Z7gemm_tnILi64ELi96ELi2ELi2ELi8ELi2ELi1EEvPKDF16_S1_PKfPfPDF16_iiiiiS3_S3_S4_.kd
    .uniform_work_group_size: 1
    .uses_dynamic_stack: false
    .vgpr_count:     100
    .vgpr_spill_count: 0
    .wavefront_size: 64
  - .agpr_count:     0
    .args:
      - .actual_access:  read_only
        .address_space:  global
        .offset:         0
        .size:           8
        .value_kind:     global_buffer
      - .actual_access:  read_only
        .address_space:  global
        .offset:         8
        .size:           8
        .value_kind:     global_buffer
      - .actual_access:  read_only
        .address_space:  global
        .offset:         16
        .size:           8
        .value_kind:     global_buffer
      - .address_space:  global
        .offset:         24
        .size:           8
        .value_kind:     global_buffer
      - .actual_access:  write_only
        .address_space:  global
        .offset:         32
        .size:           8
        .value_kind:     global_buffer
      - .offset:         40
        .size:           4
        .value_kind:     by_value
      - .offset:         44
        .size:           4
        .value_kind:     by_value
      - .offset:         48
        .size:           4
        .value_kind:     by_value
      - .offset:         52
        .size:           4
        .value_kind:     by_value
      - .offset:         56
        .size:           4
        .value_kind:     by_value
      - .actual_access:  read_only
        .address_space:  global
        .offset:         64
        .size:           8
        .value_kind:     global_buffer
      - .actual_access:  read_only
        .address_space:  global
        .offset:         72
        .size:           8
        .value_kind:     global_buffer
      - .address_space:  global
        .offset:         80
        .size:           8
        .value_kind:     global_buffer
    .group_segment_fixed_size: 8192
    .kernarg_segment_align: 8
    .kernarg_segment_size: 88
    .language:       OpenCL C
    .language_version:
      - 2
      - 0
    .max_flat_workgroup_size: 512
    .name:           _Z7gemm_tnILi128ELi192ELi2ELi4ELi3ELi6ELi1EEvPKDF16_S1_PKfPfPDF16_iiiiiS3_S3_S4_
    .private_segment_fixed_size: 0
    .sgpr_count:     46
    .sgpr_spill_count: 0
    .symbol:         _Z7gemm_tnILi128ELi192ELi2ELi4ELi3ELi6ELi1EEvPKDF16_S1_PKfPfPDF16_iiiiiS3_S3_S4_.kd
    .uniform_work_group_size: 1
    .uses_dynamic_stack: false
    .vgpr_count:     118
    .vgpr_spill_count: 0
    .wavefront_size: 64
  - .agpr_count:     24
    .args:
      - .actual_access:  read_only
        .address_space:  global
        .offset:         0
        .size:           8
        .value_kind:     global_buffer
      - .actual_access:  read_only
        .address_space:  global
        .offset:         8
        .size:           8
        .value_kind:     global_buffer
      - .actual_access:  read_only
        .address_space:  global
        .offset:         16
        .size:           8
        .value_kind:     global_buffer
      - .address_space:  global
        .offset:         24
        .size:           8
        .value_kind:     global_buffer
      - .actual_access:  write_only
        .address_space:  global
        .offset:         32
        .size:           8
        .value_kind:     global_buffer
      - .offset:         40
        .size:           4
        .value_kind:     by_value
      - .offset:         44
        .size:           4
        .value_kind:     by_value
      - .offset:         48
        .size:           4
        .value_kind:     by_value
      - .offset:         52
        .size:           4
        .value_kind:     by_value
      - .offset:         56
        .size:           4
        .value_kind:     by_value
      - .actual_access:  read_only
        .address_space:  global
        .offset:         64
        .size:           8
        .value_kind:     global_buffer
      - .actual_access:  read_only
        .address_space:  global
        .offset:         72
        .size:           8
        .value_kind:     global_buffer
      - .address_space:  global
        .offset:         80
        .size:           8
        .value_kind:     global_buffer
    .group_segment_fixed_size: 0
    .kernarg_segment_align: 8
    .kernarg_segment_size: 88
    .language:       OpenCL C
    .language_version:
      - 2
      - 0
    .max_flat_workgroup_size: 256
    .name:           _Z7gemm_tnILi64ELi96ELi2ELi2ELi8ELi5ELi1EEvPKDF16_S1_PKfPfPDF16_iiiiiS3_S3_S4_
    .private_segment_fixed_size: 0
    .sgpr_count:     52
    .sgpr_spill_count: 0
    .symbol:         _Z7gemm_tnILi64ELi96ELi2ELi2ELi8ELi5ELi1EEvPKDF16_S1_PKfPfPDF16_iiiiiS3_S3_S4_.kd
    .uniform_work_group_size: 1
    .uses_dynamic_stack: false
    .vgpr_count:     128
    .vgpr_spill_count: 0
    .wavefront_size: 64
  - .agpr_count:     0
    .args:
      - .actual_access:  read_only
        .address_space:  global
        .offset:         0
        .size:           8
        .value_kind:     global_buffer
      - .actual_access:  read_only
        .address_space:  global
        .offset:         8
        .size:           8
        .value_kind:     global_buffer
      - .actual_access:  read_only
        .address_space:  global
        .offset:         16
        .size:           8
        .value_kind:     global_buffer
      - .address_space:  global
        .offset:         24
        .size:           8
        .value_kind:     global_buffer
      - .actual_access:  read_only
        .address_space:  global
        .offset:         32
        .size:           8
        .value_kind:     global_buffer
      - .offset:         40
        .size:           4
        .value_kind:     by_value
      - .offset:         44
        .size:           4
        .value_kind:     by_value
      - .offset:         48
        .size:           4
        .value_kind:     by_value
      - .offset:         52
        .size:           4
        .value_kind:     by_value
      - .offset:         56
        .size:           4
        .value_kind:     by_value
      - .actual_access:  read_only
        .address_space:  global
        .offset:         64
        .size:           8
        .value_kind:     global_buffer
      - .actual_access:  read_only
        .address_space:  global
        .offset:         72
        .size:           8
        .value_kind:     global_buffer
      - .address_space:  global
        .offset:         80
        .size:           8
        .value_kind:     global_buffer
    .group_segment_fixed_size: 0
    .kernarg_segment_align: 8
    .kernarg_segment_size: 88
    .language:       OpenCL C
    .language_version:
      - 2
      - 0
    .max_flat_workgroup_size: 512
    .name:           _Z7gemm_tnILi128ELi192ELi2ELi4ELi3ELi3ELi4EEvPKDF16_S1_PKfPfPDF16_iiiiiS3_S3_S4_
    .private_segment_fixed_size: 0
    .sgpr_count:     40
    .sgpr_spill_count: 0
    .symbol:         _Z7gemm_tnILi128ELi192ELi2ELi4ELi3ELi3ELi4EEvPKDF16_S1_PKfPfPDF16_iiiiiS3_S3_S4_.kd
    .uniform_work_group_size: 1
    .uses_dynamic_stack: false
    .vgpr_count:     102
    .vgpr_spill_count: 0
    .wavefront_size: 64
  - .agpr_count:     0
    .args:
      - .address_space:  global
        .offset:         0
        .size:           8
        .value_kind:     global_buffer
      - .address_space:  global
        .offset:         8
        .size:           8
        .value_kind:     global_buffer
      - .address_space:  global
        .offset:         16
        .size:           8
        .value_kind:     global_buffer
      - .offset:         24
        .size:           4
        .value_kind:     by_value
      - .offset:         28
        .size:           4
        .value_kind:     by_value
      - .offset:         32
        .size:           4
        .value_kind:     by_value
      - .offset:         36
        .size:           4
        .value_kind:     by_value
      - .offset:         40
        .size:           4
        .value_kind:     by_value
    .group_segment_fixed_size: 0
    .kernarg_segment_align: 8
    .kernarg_segment_size: 44
    .language:       OpenCL C
    .language_version:
      - 2
      - 0
    .max_flat_workgroup_size: 512
    .name:           _Z17gemm_256sq_8phaseILi0EEvPKDF16_S1_Pfiiiii
    .private_segment_fixed_size: 0
    .sgpr_count:     48
    .sgpr_spill_count: 0
    .symbol:         _Z17gemm_256sq_8phaseILi0EEvPKDF16_S1_Pfiiiii.kd
    .uniform_work_group_size: 1
    .uses_dynamic_stack: false
    .vgpr_count:     244
    .vgpr_spill_count: 0
    .wavefront_size: 64
